# split-K context GEMM K-loops: all 32 fragment loads of a trip issued before the MFMAs (own destination each), counted waits
# baseline (speedup 1.0000x reference)
.LBB0_463:
	v_lshl_add_u64 v[164:165], v[80:81], 0, v[66:67]
	v_lshl_add_u64 v[166:167], v[78:79], 0, v[66:67]
	v_lshl_add_u64 v[168:169], v[76:77], 0, v[66:67]
	v_lshl_add_u64 v[170:171], v[72:73], 0, v[66:67]
	v_lshl_add_u64 v[160:161], v[74:75], 0, v[66:67]
	global_load_dwordx4 v[108:111], v[164:165], off offset:-128
	global_load_dwordx4 v[112:115], v[160:161], off offset:-128
	global_load_dwordx4 v[116:119], v[160:161], off offset:-64
	global_load_dwordx4 v[120:123], v[164:165], off offset:-64
	global_load_dwordx4 v[124:127], v[166:167], off offset:-128
	global_load_dwordx4 v[128:131], v[166:167], off offset:-64
	global_load_dwordx4 v[132:135], v[168:169], off offset:-128
	global_load_dwordx4 v[136:139], v[168:169], off offset:-64
	global_load_dwordx4 v[140:143], v[170:171], off offset:-128
	global_load_dwordx4 v[144:147], v[170:171], off offset:-64
	v_lshl_add_u64 v[162:163], v[82:83], 0, v[66:67]
	v_lshl_add_u64 v[172:173], v[86:87], 0, v[66:67]
	v_lshl_add_u64 v[174:175], v[84:85], 0, v[66:67]
	s_addk_i32 s12, 0x80
	v_lshl_add_u64 v[72:73], v[72:73], 0, s[4:5]
	v_lshl_add_u64 v[74:75], v[74:75], 0, s[4:5]
	v_lshl_add_u64 v[76:77], v[76:77], 0, s[4:5]
	v_lshl_add_u64 v[78:79], v[78:79], 0, s[4:5]
	v_lshl_add_u64 v[80:81], v[80:81], 0, s[4:5]
	v_lshl_add_u64 v[82:83], v[82:83], 0, s[4:5]
	v_lshl_add_u64 v[84:85], v[84:85], 0, s[4:5]
	s_cmpk_lt_u32 s12, 0xe0
	v_lshl_add_u64 v[86:87], v[86:87], 0, s[4:5]
	global_load_dwordx4 v[148:151], v[162:163], off offset:-128
	global_load_dwordx4 v[152:155], v[162:163], off offset:-64
	global_load_dwordx4 v[156:159], v[172:173], off offset:-128
	global_load_dwordx4 v[252:255], v[172:173], off offset:-64
	global_load_dwordx4 v[248:251], v[174:175], off offset:-128
	global_load_dwordx4 v[244:247], v[174:175], off offset:-64
	global_load_dwordx4 v[240:243], v[164:165], off
	global_load_dwordx4 v[236:239], v[160:161], off
	global_load_dwordx4 v[232:235], v[160:161], off offset:64
	global_load_dwordx4 v[228:231], v[164:165], off offset:64
	global_load_dwordx4 v[224:227], v[166:167], off
	global_load_dwordx4 v[220:223], v[166:167], off offset:64
	global_load_dwordx4 v[216:219], v[168:169], off
	global_load_dwordx4 v[212:215], v[168:169], off offset:64
	global_load_dwordx4 v[208:211], v[170:171], off
	global_load_dwordx4 v[204:207], v[170:171], off offset:64
	global_load_dwordx4 v[200:203], v[162:163], off
	global_load_dwordx4 v[196:199], v[162:163], off offset:64
	global_load_dwordx4 v[192:195], v[172:173], off
	global_load_dwordx4 v[188:191], v[172:173], off offset:64
	global_load_dwordx4 v[184:187], v[174:175], off
	global_load_dwordx4 v[180:183], v[174:175], off offset:64
	s_waitcnt vmcnt(30)
	v_mfma_f32_16x16x32_bf16 v[58:61], v[108:111], v[112:115], v[58:61]
	s_waitcnt vmcnt(27)
	v_mfma_f32_16x16x32_bf16 v[42:45], v[124:127], v[112:115], v[42:45]
	s_waitcnt vmcnt(25)
	v_mfma_f32_16x16x32_bf16 v[62:65], v[132:135], v[112:115], v[62:65]
	s_waitcnt vmcnt(23)
	v_mfma_f32_16x16x32_bf16 v[50:53], v[140:143], v[112:115], v[50:53]
	v_mfma_f32_16x16x32_bf16 v[58:61], v[120:123], v[116:119], v[58:61]
	v_mfma_f32_16x16x32_bf16 v[42:45], v[128:131], v[116:119], v[42:45]
	v_mfma_f32_16x16x32_bf16 v[62:65], v[136:139], v[116:119], v[62:65]
	s_waitcnt vmcnt(22)
	v_mfma_f32_16x16x32_bf16 v[50:53], v[144:147], v[116:119], v[50:53]
	s_waitcnt vmcnt(21)
	v_mfma_f32_16x16x32_bf16 v[34:37], v[108:111], v[148:151], v[34:37]
	v_mfma_f32_16x16x32_bf16 v[30:33], v[124:127], v[148:151], v[30:33]
	v_mfma_f32_16x16x32_bf16 v[26:29], v[132:135], v[148:151], v[26:29]
	v_mfma_f32_16x16x32_bf16 v[22:25], v[140:143], v[148:151], v[22:25]
	s_waitcnt vmcnt(20)
	v_mfma_f32_16x16x32_bf16 v[34:37], v[120:123], v[152:155], v[34:37]
	v_mfma_f32_16x16x32_bf16 v[30:33], v[128:131], v[152:155], v[30:33]
	v_mfma_f32_16x16x32_bf16 v[26:29], v[136:139], v[152:155], v[26:29]
	v_mfma_f32_16x16x32_bf16 v[22:25], v[144:147], v[152:155], v[22:25]
	s_waitcnt vmcnt(19)
	v_mfma_f32_16x16x32_bf16 v[18:21], v[108:111], v[156:159], v[18:21]
	v_mfma_f32_16x16x32_bf16 v[14:17], v[124:127], v[156:159], v[14:17]
	v_mfma_f32_16x16x32_bf16 v[10:13], v[132:135], v[156:159], v[10:13]
	v_mfma_f32_16x16x32_bf16 v[6:9], v[140:143], v[156:159], v[6:9]
	s_waitcnt vmcnt(17)
	v_mfma_f32_16x16x32_bf16 v[2:5], v[108:111], v[248:251], v[2:5]
	v_mfma_f32_16x16x32_bf16 v[54:57], v[124:127], v[248:251], v[54:57]
	v_mfma_f32_16x16x32_bf16 v[46:49], v[132:135], v[248:251], v[46:49]
	v_mfma_f32_16x16x32_bf16 v[38:41], v[140:143], v[248:251], v[38:41]
	v_mfma_f32_16x16x32_bf16 v[18:21], v[120:123], v[252:255], v[18:21]
	v_mfma_f32_16x16x32_bf16 v[14:17], v[128:131], v[252:255], v[14:17]
	v_mfma_f32_16x16x32_bf16 v[10:13], v[136:139], v[252:255], v[10:13]
	v_mfma_f32_16x16x32_bf16 v[6:9], v[144:147], v[252:255], v[6:9]
	s_waitcnt vmcnt(16)
	v_mfma_f32_16x16x32_bf16 v[2:5], v[120:123], v[244:247], v[2:5]
	v_mfma_f32_16x16x32_bf16 v[54:57], v[128:131], v[244:247], v[54:57]
	v_mfma_f32_16x16x32_bf16 v[46:49], v[136:139], v[244:247], v[46:49]
	v_mfma_f32_16x16x32_bf16 v[38:41], v[144:147], v[244:247], v[38:41]
	s_waitcnt vmcnt(14)
	v_mfma_f32_16x16x32_bf16 v[58:61], v[240:243], v[236:239], v[58:61]
	s_waitcnt vmcnt(11)
	v_mfma_f32_16x16x32_bf16 v[42:45], v[224:227], v[236:239], v[42:45]
	s_waitcnt vmcnt(9)
	v_mfma_f32_16x16x32_bf16 v[62:65], v[216:219], v[236:239], v[62:65]
	s_waitcnt vmcnt(7)
	v_mfma_f32_16x16x32_bf16 v[50:53], v[208:211], v[236:239], v[50:53]
	v_mfma_f32_16x16x32_bf16 v[58:61], v[228:231], v[232:235], v[58:61]
	v_mfma_f32_16x16x32_bf16 v[42:45], v[220:223], v[232:235], v[42:45]
	v_mfma_f32_16x16x32_bf16 v[62:65], v[212:215], v[232:235], v[62:65]
	s_waitcnt vmcnt(5)
	v_mfma_f32_16x16x32_bf16 v[34:37], v[240:243], v[200:203], v[34:37]
	v_mfma_f32_16x16x32_bf16 v[30:33], v[224:227], v[200:203], v[30:33]
	v_mfma_f32_16x16x32_bf16 v[26:29], v[216:219], v[200:203], v[26:29]
	v_mfma_f32_16x16x32_bf16 v[22:25], v[208:211], v[200:203], v[22:25]
	s_waitcnt vmcnt(3)
	v_mfma_f32_16x16x32_bf16 v[18:21], v[240:243], v[192:195], v[18:21]
	v_mfma_f32_16x16x32_bf16 v[14:17], v[224:227], v[192:195], v[14:17]
	v_mfma_f32_16x16x32_bf16 v[10:13], v[216:219], v[192:195], v[10:13]
	v_mfma_f32_16x16x32_bf16 v[6:9], v[208:211], v[192:195], v[6:9]
	s_waitcnt vmcnt(1)
	v_mfma_f32_16x16x32_bf16 v[2:5], v[240:243], v[184:187], v[2:5]
	v_mfma_f32_16x16x32_bf16 v[54:57], v[224:227], v[184:187], v[54:57]
	v_mfma_f32_16x16x32_bf16 v[46:49], v[216:219], v[184:187], v[46:49]
	v_mfma_f32_16x16x32_bf16 v[38:41], v[208:211], v[184:187], v[38:41]
	v_mfma_f32_16x16x32_bf16 v[50:53], v[204:207], v[232:235], v[50:53]
	v_mfma_f32_16x16x32_bf16 v[34:37], v[228:231], v[196:199], v[34:37]
	v_mfma_f32_16x16x32_bf16 v[30:33], v[220:223], v[196:199], v[30:33]
	v_mfma_f32_16x16x32_bf16 v[26:29], v[212:215], v[196:199], v[26:29]
	v_mfma_f32_16x16x32_bf16 v[22:25], v[204:207], v[196:199], v[22:25]
	v_mfma_f32_16x16x32_bf16 v[18:21], v[228:231], v[188:191], v[18:21]
	v_mfma_f32_16x16x32_bf16 v[14:17], v[220:223], v[188:191], v[14:17]
	v_mfma_f32_16x16x32_bf16 v[10:13], v[212:215], v[188:191], v[10:13]
	v_mfma_f32_16x16x32_bf16 v[6:9], v[204:207], v[188:191], v[6:9]
	s_waitcnt vmcnt(0)
	v_mfma_f32_16x16x32_bf16 v[2:5], v[228:231], v[180:183], v[2:5]
	v_mfma_f32_16x16x32_bf16 v[54:57], v[220:223], v[180:183], v[54:57]
	v_mfma_f32_16x16x32_bf16 v[46:49], v[212:215], v[180:183], v[46:49]
	v_mfma_f32_16x16x32_bf16 v[38:41], v[204:207], v[180:183], v[38:41]
	s_cbranch_scc1 .LBB0_463
	s_barrier
	ds_write_b128 v106, v[58:61]
	ds_write_b128 v106, v[42:45] offset:16
	ds_write_b128 v106, v[62:65] offset:128
	ds_write_b128 v106, v[50:53] offset:144
	ds_write_b128 v106, v[34:37] offset:4096
	ds_write_b128 v106, v[30:33] offset:4112
	ds_write_b128 v106, v[26:29] offset:4224
	ds_write_b128 v106, v[22:25] offset:4240
	ds_write_b128 v106, v[18:21] offset:8192
	ds_write_b128 v106, v[14:17] offset:8208
	ds_write_b128 v106, v[10:13] offset:8320
	ds_write_b128 v106, v[6:9] offset:8336
	ds_write_b128 v106, v[2:5] offset:12288
	ds_write_b128 v106, v[54:57] offset:12304
	ds_write_b128 v106, v[46:49] offset:12416
	ds_write_b128 v106, v[38:41] offset:12432
	s_waitcnt lgkmcnt(0)
	s_barrier
	ds_read_b128 v[2:5], v89
	ds_read_b128 v[6:9], v89 offset:16
	ds_read_b128 v[10:13], v89 offset:16384
	s_lshl_b32 s11, s11, 6
	s_sub_i32 s11, s9, s11
	s_waitcnt lgkmcnt(2)
	v_pk_add_f32 v[14:15], v[4:5], 0 op_sel_hi:[1,0]
	v_pk_add_f32 v[16:17], v[2:3], 0 op_sel_hi:[1,0]
	ds_read_b128 v[2:5], v89 offset:16400
	s_waitcnt lgkmcnt(2)
	v_pk_add_f32 v[18:19], v[8:9], 0 op_sel_hi:[1,0]
	v_pk_add_f32 v[20:21], v[6:7], 0 op_sel_hi:[1,0]
	ds_read_b128 v[6:9], v89 offset:32768
	s_waitcnt lgkmcnt(2)
	v_pk_add_f32 v[14:15], v[14:15], v[12:13]
	v_pk_add_f32 v[16:17], v[16:17], v[10:11]
	s_waitcnt lgkmcnt(1)
	v_pk_add_f32 v[18:19], v[18:19], v[4:5]
	ds_read_b128 v[10:13], v89 offset:32784
	v_pk_add_f32 v[20:21], v[20:21], v[2:3]
	ds_read_b128 v[2:5], v89 offset:49152
	s_waitcnt lgkmcnt(2)
	v_pk_add_f32 v[14:15], v[14:15], v[8:9]
	v_pk_add_f32 v[16:17], v[16:17], v[6:7]
	ds_read_b128 v[6:9], v89 offset:49168
	s_waitcnt lgkmcnt(2)
	v_pk_add_f32 v[18:19], v[18:19], v[12:13]
	v_pk_add_f32 v[20:21], v[20:21], v[10:11]
	s_waitcnt lgkmcnt(1)
	v_pk_add_f32 v[14:15], v[14:15], v[4:5]
	ds_read_b128 v[10:13], v90
	v_pk_add_f32 v[16:17], v[16:17], v[2:3]
	ds_read_b128 v[2:5], v91
	s_waitcnt lgkmcnt(2)
	v_pk_add_f32 v[18:19], v[18:19], v[8:9]
	v_pk_add_f32 v[20:21], v[20:21], v[6:7]
	ds_read_b128 v[6:9], v92
	s_waitcnt lgkmcnt(2)
	v_pk_add_f32 v[14:15], v[14:15], v[12:13]
	v_pk_add_f32 v[16:17], v[16:17], v[10:11]
	s_waitcnt lgkmcnt(1)
	v_pk_add_f32 v[18:19], v[18:19], v[4:5]
	ds_read_b128 v[10:13], v93
	v_pk_add_f32 v[20:21], v[20:21], v[2:3]
	ds_read_b128 v[2:5], v94
	s_waitcnt lgkmcnt(2)
	v_pk_add_f32 v[14:15], v[14:15], v[8:9]
	v_pk_add_f32 v[16:17], v[16:17], v[6:7]
	ds_read_b128 v[6:9], v95
	s_waitcnt lgkmcnt(2)
	v_pk_add_f32 v[18:19], v[18:19], v[12:13]
	v_pk_add_f32 v[20:21], v[20:21], v[10:11]
	s_waitcnt lgkmcnt(1)
	v_pk_add_f32 v[4:5], v[14:15], v[4:5]
	ds_read_b128 v[10:13], v96
	v_pk_add_f32 v[22:23], v[16:17], v[2:3]
	ds_read_b128 v[14:17], v97
	s_ashr_i32 s12, s11, 2
	s_waitcnt lgkmcnt(2)
	v_pk_add_f32 v[8:9], v[18:19], v[8:9]
	v_pk_add_f32 v[18:19], v[20:21], v[6:7]
	s_add_i32 s12, s12, -5
	s_waitcnt lgkmcnt(1)
	v_pk_add_f32 v[2:3], v[4:5], v[12:13]
	v_pk_add_f32 v[4:5], v[22:23], v[10:11]
	s_waitcnt lgkmcnt(0)
	v_pk_add_f32 v[6:7], v[8:9], v[16:17]
	s_cmp_gt_u32 s12, 3
	v_pk_add_f32 v[8:9], v[18:19], v[14:15]
	s_cbranch_scc1 .LBB0_461
	v_mul_f32_e32 v10, 0x3dd2d3e8, v4
	v_mul_f32_e32 v11, 0x3dd2d3e8, v5
	v_mul_f32_e32 v12, 0x3dd2d3e8, v2
	v_mul_f32_e32 v13, 0x3dd2d3e8, v3
	v_mul_f32_e32 v14, 0x3dd2d3e8, v8
	v_mul_f32_e32 v15, 0x3dd2d3e8, v9
	v_mul_f32_e32 v16, 0x3dd2d3e8, v6
	v_mul_f32_e32 v17, 0x3dd2d3e8, v7
	v_fmaak_f32 v10, v4, v10, 0x40135761
	v_fmaak_f32 v11, v5, v11, 0x40135761
	v_fmaak_f32 v12, v2, v12, 0x40135761
	v_fmaak_f32 v13, v3, v13, 0x40135761
	v_fmaak_f32 v14, v8, v14, 0x40135761
	v_fmaak_f32 v15, v9, v15, 0x40135761
	v_fmaak_f32 v16, v6, v16, 0x40135761
	v_fmaak_f32 v17, v7, v17, 0x40135761
	v_mul_f32_e64 v10, v4, -v10
	v_mul_f32_e64 v11, v5, -v11
	v_mul_f32_e64 v12, v2, -v12
	v_mul_f32_e64 v13, v3, -v13
	v_mul_f32_e64 v14, v8, -v14
	v_mul_f32_e64 v15, v9, -v15
	v_mul_f32_e64 v16, v6, -v16
	v_mul_f32_e64 v17, v7, -v17
	v_exp_f32_e32 v10, v10
	v_exp_f32_e32 v11, v11
	v_exp_f32_e32 v12, v12
	v_exp_f32_e32 v13, v13
	v_exp_f32_e32 v14, v14
	v_exp_f32_e32 v15, v15
	v_exp_f32_e32 v16, v16
	v_exp_f32_e32 v17, v17
	v_add_f32_e32 v10, 1.0, v10
	v_add_f32_e32 v11, 1.0, v11
	v_add_f32_e32 v12, 1.0, v12
	v_add_f32_e32 v13, 1.0, v13
	v_add_f32_e32 v14, 1.0, v14
	v_add_f32_e32 v15, 1.0, v15
	v_add_f32_e32 v16, 1.0, v16
	v_add_f32_e32 v17, 1.0, v17
	v_rcp_f32_e32 v10, v10
	v_rcp_f32_e32 v11, v11
	v_rcp_f32_e32 v12, v12
	v_rcp_f32_e32 v13, v13
	v_rcp_f32_e32 v14, v14
	v_rcp_f32_e32 v15, v15
	v_rcp_f32_e32 v16, v16
	v_rcp_f32_e32 v17, v17
	v_pk_mul_f32 v[4:5], v[4:5], v[10:11]
	v_pk_mul_f32 v[2:3], v[2:3], v[12:13]
	v_pk_mul_f32 v[8:9], v[8:9], v[14:15]
	v_pk_mul_f32 v[6:7], v[6:7], v[16:17]
	s_branch .LBB0_461

.LBB0_1536:
	v_lshl_add_u64 v[168:169], v[82:83], 0, v[66:67]
	v_lshl_add_u64 v[170:171], v[80:81], 0, v[66:67]
	v_lshl_add_u64 v[172:173], v[78:79], 0, v[66:67]
	v_lshl_add_u64 v[174:175], v[74:75], 0, v[66:67]
	v_lshl_add_u64 v[164:165], v[76:77], 0, v[66:67]
	global_load_dwordx4 v[112:115], v[168:169], off offset:-128
	global_load_dwordx4 v[116:119], v[164:165], off offset:-128
	global_load_dwordx4 v[120:123], v[164:165], off offset:-64
	global_load_dwordx4 v[124:127], v[168:169], off offset:-64
	global_load_dwordx4 v[128:131], v[170:171], off offset:-128
	global_load_dwordx4 v[132:135], v[170:171], off offset:-64
	global_load_dwordx4 v[136:139], v[172:173], off offset:-128
	global_load_dwordx4 v[140:143], v[172:173], off offset:-64
	global_load_dwordx4 v[144:147], v[174:175], off offset:-128
	global_load_dwordx4 v[148:151], v[174:175], off offset:-64
	v_lshl_add_u64 v[166:167], v[84:85], 0, v[66:67]
	v_lshl_add_u64 v[176:177], v[88:89], 0, v[66:67]
	v_lshl_add_u64 v[178:179], v[86:87], 0, v[66:67]
	s_addk_i32 s11, 0x80
	v_lshl_add_u64 v[74:75], v[74:75], 0, s[6:7]
	v_lshl_add_u64 v[76:77], v[76:77], 0, s[6:7]
	v_lshl_add_u64 v[78:79], v[78:79], 0, s[6:7]
	v_lshl_add_u64 v[80:81], v[80:81], 0, s[6:7]
	v_lshl_add_u64 v[82:83], v[82:83], 0, s[6:7]
	v_lshl_add_u64 v[84:85], v[84:85], 0, s[6:7]
	v_lshl_add_u64 v[86:87], v[86:87], 0, s[6:7]
	s_cmpk_lt_u32 s11, 0xe0
	v_lshl_add_u64 v[88:89], v[88:89], 0, s[6:7]
	global_load_dwordx4 v[152:155], v[166:167], off offset:-128
	global_load_dwordx4 v[156:159], v[166:167], off offset:-64
	global_load_dwordx4 v[160:163], v[176:177], off offset:-128
	global_load_dwordx4 v[252:255], v[176:177], off offset:-64
	global_load_dwordx4 v[248:251], v[178:179], off offset:-128
	global_load_dwordx4 v[244:247], v[178:179], off offset:-64
	global_load_dwordx4 v[240:243], v[168:169], off
	global_load_dwordx4 v[236:239], v[164:165], off
	global_load_dwordx4 v[232:235], v[164:165], off offset:64
	global_load_dwordx4 v[228:231], v[168:169], off offset:64
	global_load_dwordx4 v[224:227], v[170:171], off
	global_load_dwordx4 v[220:223], v[170:171], off offset:64
	global_load_dwordx4 v[216:219], v[172:173], off
	global_load_dwordx4 v[212:215], v[172:173], off offset:64
	global_load_dwordx4 v[208:211], v[174:175], off
	global_load_dwordx4 v[204:207], v[174:175], off offset:64
	global_load_dwordx4 v[200:203], v[166:167], off
	global_load_dwordx4 v[196:199], v[166:167], off offset:64
	global_load_dwordx4 v[192:195], v[176:177], off
	global_load_dwordx4 v[188:191], v[176:177], off offset:64
	global_load_dwordx4 v[184:187], v[178:179], off
	global_load_dwordx4 v[180:183], v[178:179], off offset:64
	s_waitcnt vmcnt(30)
	v_mfma_f32_16x16x32_bf16 v[62:65], v[112:115], v[116:119], v[62:65]
	s_waitcnt vmcnt(27)
	v_mfma_f32_16x16x32_bf16 v[54:57], v[128:131], v[116:119], v[54:57]
	s_waitcnt vmcnt(25)
	v_mfma_f32_16x16x32_bf16 v[58:61], v[136:139], v[116:119], v[58:61]
	s_waitcnt vmcnt(23)
	v_mfma_f32_16x16x32_bf16 v[50:53], v[144:147], v[116:119], v[50:53]
	v_mfma_f32_16x16x32_bf16 v[62:65], v[124:127], v[120:123], v[62:65]
	v_mfma_f32_16x16x32_bf16 v[54:57], v[132:135], v[120:123], v[54:57]
	v_mfma_f32_16x16x32_bf16 v[58:61], v[140:143], v[120:123], v[58:61]
	s_waitcnt vmcnt(22)
	v_mfma_f32_16x16x32_bf16 v[50:53], v[148:151], v[120:123], v[50:53]
	s_waitcnt vmcnt(21)
	v_mfma_f32_16x16x32_bf16 v[46:49], v[112:115], v[152:155], v[46:49]
	v_mfma_f32_16x16x32_bf16 v[42:45], v[128:131], v[152:155], v[42:45]
	v_mfma_f32_16x16x32_bf16 v[38:41], v[136:139], v[152:155], v[38:41]
	v_mfma_f32_16x16x32_bf16 v[34:37], v[144:147], v[152:155], v[34:37]
	s_waitcnt vmcnt(20)
	v_mfma_f32_16x16x32_bf16 v[46:49], v[124:127], v[156:159], v[46:49]
	v_mfma_f32_16x16x32_bf16 v[42:45], v[132:135], v[156:159], v[42:45]
	v_mfma_f32_16x16x32_bf16 v[38:41], v[140:143], v[156:159], v[38:41]
	v_mfma_f32_16x16x32_bf16 v[34:37], v[148:151], v[156:159], v[34:37]
	s_waitcnt vmcnt(19)
	v_mfma_f32_16x16x32_bf16 v[26:29], v[112:115], v[160:163], v[26:29]
	v_mfma_f32_16x16x32_bf16 v[18:21], v[128:131], v[160:163], v[18:21]
	v_mfma_f32_16x16x32_bf16 v[14:17], v[136:139], v[160:163], v[14:17]
	v_mfma_f32_16x16x32_bf16 v[6:9], v[144:147], v[160:163], v[6:9]
	s_waitcnt vmcnt(17)
	v_mfma_f32_16x16x32_bf16 v[2:5], v[112:115], v[248:251], v[2:5]
	v_mfma_f32_16x16x32_bf16 v[30:33], v[128:131], v[248:251], v[30:33]
	v_mfma_f32_16x16x32_bf16 v[22:25], v[136:139], v[248:251], v[22:25]
	v_mfma_f32_16x16x32_bf16 v[10:13], v[144:147], v[248:251], v[10:13]
	v_mfma_f32_16x16x32_bf16 v[26:29], v[124:127], v[252:255], v[26:29]
	v_mfma_f32_16x16x32_bf16 v[18:21], v[132:135], v[252:255], v[18:21]
	v_mfma_f32_16x16x32_bf16 v[14:17], v[140:143], v[252:255], v[14:17]
	v_mfma_f32_16x16x32_bf16 v[6:9], v[148:151], v[252:255], v[6:9]
	s_waitcnt vmcnt(16)
	v_mfma_f32_16x16x32_bf16 v[2:5], v[124:127], v[244:247], v[2:5]
	v_mfma_f32_16x16x32_bf16 v[30:33], v[132:135], v[244:247], v[30:33]
	v_mfma_f32_16x16x32_bf16 v[22:25], v[140:143], v[244:247], v[22:25]
	v_mfma_f32_16x16x32_bf16 v[10:13], v[148:151], v[244:247], v[10:13]
	s_waitcnt vmcnt(14)
	v_mfma_f32_16x16x32_bf16 v[62:65], v[240:243], v[236:239], v[62:65]
	s_waitcnt vmcnt(11)
	v_mfma_f32_16x16x32_bf16 v[54:57], v[224:227], v[236:239], v[54:57]
	s_waitcnt vmcnt(9)
	v_mfma_f32_16x16x32_bf16 v[58:61], v[216:219], v[236:239], v[58:61]
	s_waitcnt vmcnt(7)
	v_mfma_f32_16x16x32_bf16 v[50:53], v[208:211], v[236:239], v[50:53]
	v_mfma_f32_16x16x32_bf16 v[62:65], v[228:231], v[232:235], v[62:65]
	v_mfma_f32_16x16x32_bf16 v[54:57], v[220:223], v[232:235], v[54:57]
	v_mfma_f32_16x16x32_bf16 v[58:61], v[212:215], v[232:235], v[58:61]
	s_waitcnt vmcnt(5)
	v_mfma_f32_16x16x32_bf16 v[46:49], v[240:243], v[200:203], v[46:49]
	v_mfma_f32_16x16x32_bf16 v[42:45], v[224:227], v[200:203], v[42:45]
	v_mfma_f32_16x16x32_bf16 v[38:41], v[216:219], v[200:203], v[38:41]
	v_mfma_f32_16x16x32_bf16 v[34:37], v[208:211], v[200:203], v[34:37]
	s_waitcnt vmcnt(3)
	v_mfma_f32_16x16x32_bf16 v[26:29], v[240:243], v[192:195], v[26:29]
	v_mfma_f32_16x16x32_bf16 v[18:21], v[224:227], v[192:195], v[18:21]
	v_mfma_f32_16x16x32_bf16 v[14:17], v[216:219], v[192:195], v[14:17]
	v_mfma_f32_16x16x32_bf16 v[6:9], v[208:211], v[192:195], v[6:9]
	s_waitcnt vmcnt(1)
	v_mfma_f32_16x16x32_bf16 v[2:5], v[240:243], v[184:187], v[2:5]
	v_mfma_f32_16x16x32_bf16 v[30:33], v[224:227], v[184:187], v[30:33]
	v_mfma_f32_16x16x32_bf16 v[22:25], v[216:219], v[184:187], v[22:25]
	v_mfma_f32_16x16x32_bf16 v[10:13], v[208:211], v[184:187], v[10:13]
	v_mfma_f32_16x16x32_bf16 v[50:53], v[204:207], v[232:235], v[50:53]
	v_mfma_f32_16x16x32_bf16 v[46:49], v[228:231], v[196:199], v[46:49]
	v_mfma_f32_16x16x32_bf16 v[42:45], v[220:223], v[196:199], v[42:45]
	v_mfma_f32_16x16x32_bf16 v[38:41], v[212:215], v[196:199], v[38:41]
	v_mfma_f32_16x16x32_bf16 v[34:37], v[204:207], v[196:199], v[34:37]
	v_mfma_f32_16x16x32_bf16 v[26:29], v[228:231], v[188:191], v[26:29]
	v_mfma_f32_16x16x32_bf16 v[18:21], v[220:223], v[188:191], v[18:21]
	v_mfma_f32_16x16x32_bf16 v[14:17], v[212:215], v[188:191], v[14:17]
	v_mfma_f32_16x16x32_bf16 v[6:9], v[204:207], v[188:191], v[6:9]
	s_waitcnt vmcnt(0)
	v_mfma_f32_16x16x32_bf16 v[2:5], v[228:231], v[180:183], v[2:5]
	v_mfma_f32_16x16x32_bf16 v[30:33], v[220:223], v[180:183], v[30:33]
	v_mfma_f32_16x16x32_bf16 v[22:25], v[212:215], v[180:183], v[22:25]
	v_mfma_f32_16x16x32_bf16 v[10:13], v[204:207], v[180:183], v[10:13]
	s_cbranch_scc1 .LBB0_1536
	s_lshl_b32 s16, s17, 5
	s_sub_i32 s16, s10, s16
	s_add_i32 s11, s18, 0x4000
	s_lshr_b32 s18, s18, 4
	s_lshl_b32 s20, s16, 1
	s_ashr_i32 s19, s11, 8
	s_and_b32 s18, s18, 4
	s_and_b32 s20, s20, 2
	v_add_u32_e32 v68, s19, v90
	s_ashr_i32 s19, s16, 2
	s_or_b32 s18, s20, s18
	s_lshl_b32 s17, s17, 8
	v_lshl_add_u32 v74, v68, 3, s19
	s_lshl_b32 s18, s18, 10
	s_and_b32 s19, s17, 0x200
	s_lshl_b32 s20, s16, 5
	s_or_b32 s17, s19, s18
	v_and_or_b32 v111, s20, 64, v1
	v_or_b32_e32 v68, s17, v111
	s_or_b32 s17, s18, 0x400
	v_lshlrev_b32_e32 v68, 3, v68
	s_or_b32 s20, s19, s17
	v_ashrrev_i32_e32 v75, 31, v74
	v_lshl_add_u64 v[76:77], s[14:15], 0, v[68:69]
	v_or_b32_e32 v68, s20, v111
	v_lshlrev_b64 v[74:75], 16, v[74:75]
	v_lshlrev_b32_e32 v68, 3, v68
	v_lshl_add_u64 v[76:77], v[76:77], 0, v[74:75]
	v_lshl_add_u64 v[78:79], s[14:15], 0, v[68:69]
	global_load_dwordx2 v[76:77], v[76:77], off
	v_lshl_add_u64 v[78:79], v[78:79], 0, v[74:75]
	global_load_dwordx2 v[78:79], v[78:79], off
	s_or_b32 s20, s19, 0x80
	s_or_b32 s21, s20, s18
	v_or_b32_e32 v68, s21, v111
	v_lshlrev_b32_e32 v68, 3, v68
	v_lshl_add_u64 v[80:81], s[14:15], 0, v[68:69]
	v_lshl_add_u64 v[80:81], v[80:81], 0, v[74:75]
	s_or_b32 s20, s20, s17
	global_load_dwordx2 v[80:81], v[80:81], off
	v_or_b32_e32 v68, s20, v111
	v_lshlrev_b32_e32 v68, 3, v68
	v_lshl_add_u64 v[82:83], s[14:15], 0, v[68:69]
	s_or_b32 s20, s19, 0x100
	v_lshl_add_u64 v[82:83], v[82:83], 0, v[74:75]
	s_or_b32 s21, s20, s18
	global_load_dwordx2 v[82:83], v[82:83], off
	v_or_b32_e32 v68, s21, v111
	v_lshlrev_b32_e32 v68, 3, v68
	v_lshl_add_u64 v[84:85], s[14:15], 0, v[68:69]
	v_lshl_add_u64 v[84:85], v[84:85], 0, v[74:75]
	s_or_b32 s19, s19, 0x180
	s_or_b32 s20, s20, s17
	global_load_dwordx2 v[84:85], v[84:85], off
	s_or_b32 s18, s19, s18
	v_or_b32_e32 v68, s20, v111
	v_or_b32_e32 v88, s18, v111
	v_lshlrev_b32_e32 v68, 3, v68
	v_lshl_add_u64 v[86:87], s[14:15], 0, v[68:69]
	v_lshlrev_b32_e32 v68, 3, v88
	v_lshl_add_u64 v[86:87], v[86:87], 0, v[74:75]
	v_lshl_add_u64 v[88:89], s[14:15], 0, v[68:69]
	v_lshl_add_u64 v[88:89], v[88:89], 0, v[74:75]
	global_load_dwordx2 v[112:113], v[86:87], off
	global_load_dwordx2 v[114:115], v[88:89], off
	s_or_b32 s17, s19, s17
	v_or_b32_e32 v68, s17, v111
	v_lshlrev_b32_e32 v68, 3, v68
	s_add_i32 s10, s10, s28
	s_cmpk_lt_i32 s10, 0x100
	s_waitcnt vmcnt(6)
	v_cvt_f32_ubyte1_e32 v89, v76
	v_cvt_f32_ubyte0_e32 v88, v76
	v_cvt_f32_ubyte1_e32 v119, v77
	v_cvt_f32_ubyte0_e32 v118, v77
	v_cvt_f32_ubyte3_e32 v87, v76
	v_cvt_f32_ubyte2_e32 v86, v76
	v_cvt_f32_ubyte3_e32 v117, v77
	v_cvt_f32_ubyte2_e32 v116, v77
	v_pk_mul_f32 v[76:77], v[88:89], s[8:9] op_sel_hi:[1,0]
	v_pk_mul_f32 v[88:89], v[118:119], s[8:9] op_sel_hi:[1,0]
	s_waitcnt vmcnt(5)
	v_cvt_f32_ubyte3_e32 v119, v78
	v_cvt_f32_ubyte2_e32 v118, v78
	v_cvt_f32_ubyte1_e32 v121, v78
	v_cvt_f32_ubyte0_e32 v120, v78
	v_cvt_f32_ubyte3_e32 v123, v79
	v_cvt_f32_ubyte2_e32 v122, v79
	v_cvt_f32_ubyte1_e32 v125, v79
	v_cvt_f32_ubyte0_e32 v124, v79
	v_pk_mul_f32 v[78:79], v[118:119], s[8:9] op_sel_hi:[1,0]
	v_pk_mul_f32 v[62:63], v[62:63], v[76:77]
	v_pk_mul_f32 v[60:61], v[60:61], v[78:79]
	v_lshl_add_u64 v[78:79], s[14:15], 0, v[68:69]
	v_lshl_add_u64 v[74:75], v[78:79], 0, v[74:75]
	global_load_dwordx2 v[74:75], v[74:75], off
	v_pk_mul_f32 v[76:77], v[120:121], s[8:9] op_sel_hi:[1,0]
	s_waitcnt vmcnt(5)
	v_cvt_f32_ubyte1_e32 v79, v80
	v_pk_mul_f32 v[58:59], v[58:59], v[76:77]
	v_cvt_f32_ubyte3_e32 v77, v80
	v_cvt_f32_ubyte2_e32 v76, v80
	v_cvt_f32_ubyte0_e32 v78, v80
	v_pk_mul_f32 v[78:79], v[78:79], s[8:9] op_sel_hi:[1,0]
	v_pk_mul_f32 v[76:77], v[76:77], s[8:9] op_sel_hi:[1,0]
	v_pk_mul_f32 v[46:47], v[46:47], v[78:79]
	v_pk_mul_f32 v[48:49], v[48:49], v[76:77]
	v_cvt_f32_ubyte3_e32 v77, v81
	v_cvt_f32_ubyte2_e32 v76, v81
	v_cvt_f32_ubyte1_e32 v79, v81
	v_cvt_f32_ubyte0_e32 v78, v81
	v_pk_mul_f32 v[78:79], v[78:79], s[8:9] op_sel_hi:[1,0]
	v_pk_mul_f32 v[76:77], v[76:77], s[8:9] op_sel_hi:[1,0]
	v_pk_mul_f32 v[42:43], v[42:43], v[78:79]
	v_pk_mul_f32 v[44:45], v[44:45], v[76:77]
	s_waitcnt vmcnt(4)
	v_cvt_f32_ubyte3_e32 v77, v82
	v_cvt_f32_ubyte2_e32 v76, v82
	v_cvt_f32_ubyte1_e32 v79, v82
	v_cvt_f32_ubyte0_e32 v78, v82
	v_pk_mul_f32 v[78:79], v[78:79], s[8:9] op_sel_hi:[1,0]
	v_pk_mul_f32 v[76:77], v[76:77], s[8:9] op_sel_hi:[1,0]
	v_pk_mul_f32 v[38:39], v[38:39], v[78:79]
	v_pk_mul_f32 v[40:41], v[40:41], v[76:77]
	v_cvt_f32_ubyte3_e32 v77, v83
	v_cvt_f32_ubyte2_e32 v76, v83
	v_cvt_f32_ubyte1_e32 v79, v83
	v_cvt_f32_ubyte0_e32 v78, v83
	v_pk_mul_f32 v[78:79], v[78:79], s[8:9] op_sel_hi:[1,0]
	v_pk_mul_f32 v[76:77], v[76:77], s[8:9] op_sel_hi:[1,0]
	v_pk_mul_f32 v[34:35], v[34:35], v[78:79]
	v_pk_mul_f32 v[36:37], v[36:37], v[76:77]
	s_waitcnt vmcnt(3)
	v_cvt_f32_ubyte3_e32 v77, v84
	v_cvt_f32_ubyte2_e32 v76, v84
	v_cvt_f32_ubyte1_e32 v79, v84
	v_cvt_f32_ubyte0_e32 v78, v84
	v_pk_mul_f32 v[78:79], v[78:79], s[8:9] op_sel_hi:[1,0]
	v_pk_mul_f32 v[76:77], v[76:77], s[8:9] op_sel_hi:[1,0]
	v_pk_mul_f32 v[26:27], v[26:27], v[78:79]
	v_pk_mul_f32 v[28:29], v[28:29], v[76:77]
	v_cvt_f32_ubyte3_e32 v77, v85
	v_cvt_f32_ubyte2_e32 v76, v85
	v_cvt_f32_ubyte1_e32 v79, v85
	v_cvt_f32_ubyte0_e32 v78, v85
	v_pk_mul_f32 v[78:79], v[78:79], s[8:9] op_sel_hi:[1,0]
	v_pk_mul_f32 v[76:77], v[76:77], s[8:9] op_sel_hi:[1,0]
	v_pk_mul_f32 v[18:19], v[18:19], v[78:79]
	v_pk_mul_f32 v[20:21], v[20:21], v[76:77]
	s_waitcnt vmcnt(2)
	v_cvt_f32_ubyte3_e32 v77, v112
	v_cvt_f32_ubyte2_e32 v76, v112
	v_cvt_f32_ubyte1_e32 v79, v112
	v_cvt_f32_ubyte0_e32 v78, v112
	v_pk_mul_f32 v[78:79], v[78:79], s[8:9] op_sel_hi:[1,0]
	v_pk_mul_f32 v[76:77], v[76:77], s[8:9] op_sel_hi:[1,0]
	v_pk_mul_f32 v[14:15], v[14:15], v[78:79]
	v_pk_mul_f32 v[16:17], v[16:17], v[76:77]
	v_cvt_f32_ubyte3_e32 v77, v113
	v_cvt_f32_ubyte2_e32 v76, v113
	v_cvt_f32_ubyte1_e32 v79, v113
	v_cvt_f32_ubyte0_e32 v78, v113
	v_pk_mul_f32 v[78:79], v[78:79], s[8:9] op_sel_hi:[1,0]
	v_pk_mul_f32 v[76:77], v[76:77], s[8:9] op_sel_hi:[1,0]
	v_pk_mul_f32 v[6:7], v[6:7], v[78:79]
	v_pk_mul_f32 v[8:9], v[8:9], v[76:77]
	s_waitcnt vmcnt(1)
	v_cvt_f32_ubyte3_e32 v77, v114
	v_cvt_f32_ubyte2_e32 v76, v114
	v_cvt_f32_ubyte1_e32 v79, v114
	v_cvt_f32_ubyte0_e32 v78, v114
	v_pk_mul_f32 v[78:79], v[78:79], s[8:9] op_sel_hi:[1,0]
	v_pk_mul_f32 v[76:77], v[76:77], s[8:9] op_sel_hi:[1,0]
	v_pk_mul_f32 v[2:3], v[2:3], v[78:79]
	v_pk_mul_f32 v[4:5], v[4:5], v[76:77]
	v_cvt_f32_ubyte3_e32 v77, v115
	v_cvt_f32_ubyte2_e32 v76, v115
	v_cvt_f32_ubyte1_e32 v79, v115
	v_cvt_f32_ubyte0_e32 v78, v115
	v_pk_mul_f32 v[78:79], v[78:79], s[8:9] op_sel_hi:[1,0]
	v_pk_mul_f32 v[76:77], v[76:77], s[8:9] op_sel_hi:[1,0]
	v_pk_mul_f32 v[30:31], v[30:31], v[78:79]
	v_pk_mul_f32 v[32:33], v[32:33], v[76:77]
	s_waitcnt vmcnt(0)
	v_cvt_f32_ubyte3_e32 v77, v74
	v_cvt_f32_ubyte2_e32 v76, v74
	v_cvt_f32_ubyte1_e32 v79, v74
	v_cvt_f32_ubyte0_e32 v78, v74
	v_pk_mul_f32 v[78:79], v[78:79], s[8:9] op_sel_hi:[1,0]
	v_pk_mul_f32 v[76:77], v[76:77], s[8:9] op_sel_hi:[1,0]
	v_pk_mul_f32 v[86:87], v[86:87], s[8:9] op_sel_hi:[1,0]
	v_pk_mul_f32 v[24:25], v[24:25], v[76:77]
	v_pk_mul_f32 v[22:23], v[22:23], v[78:79]
	v_cvt_f32_ubyte3_e32 v77, v75
	v_cvt_f32_ubyte2_e32 v76, v75
	v_cvt_f32_ubyte1_e32 v79, v75
	v_cvt_f32_ubyte0_e32 v78, v75
	v_pk_mul_f32 v[116:117], v[116:117], s[8:9] op_sel_hi:[1,0]
	v_pk_mul_f32 v[64:65], v[64:65], v[86:87]
	v_pk_mul_f32 v[54:55], v[54:55], v[88:89]
	v_pk_mul_f32 v[86:87], v[124:125], s[8:9] op_sel_hi:[1,0]
	v_pk_mul_f32 v[88:89], v[122:123], s[8:9] op_sel_hi:[1,0]
	v_pk_mul_f32 v[74:75], v[78:79], s[8:9] op_sel_hi:[1,0]
	v_pk_mul_f32 v[76:77], v[76:77], s[8:9] op_sel_hi:[1,0]
	v_pk_mul_f32 v[56:57], v[56:57], v[116:117]
	v_pk_mul_f32 v[52:53], v[52:53], v[88:89]
	v_pk_mul_f32 v[50:51], v[50:51], v[86:87]
	v_pk_mul_f32 v[12:13], v[12:13], v[76:77]
	v_pk_mul_f32 v[10:11], v[10:11], v[74:75]
	s_barrier
	ds_write_b128 v110, v[62:65]
	ds_write_b128 v110, v[54:57] offset:16
	ds_write_b128 v110, v[58:61] offset:128
	ds_write_b128 v110, v[50:53] offset:144
	ds_write_b128 v110, v[46:49] offset:4096
	ds_write_b128 v110, v[42:45] offset:4112
	ds_write_b128 v110, v[38:41] offset:4224
	ds_write_b128 v110, v[34:37] offset:4240
	ds_write_b128 v110, v[26:29] offset:8192
	ds_write_b128 v110, v[18:21] offset:8208
	ds_write_b128 v110, v[14:17] offset:8320
	ds_write_b128 v110, v[6:9] offset:8336
	ds_write_b128 v110, v[2:5] offset:12288
	ds_write_b128 v110, v[30:33] offset:12304
	ds_write_b128 v110, v[22:25] offset:12416
	ds_write_b128 v110, v[10:13] offset:12432
	s_waitcnt lgkmcnt(0)
	s_barrier
	ds_read_b128 v[2:5], v93
	ds_read_b128 v[6:9], v93 offset:16
	ds_read_b128 v[10:13], v93 offset:16384
	s_waitcnt lgkmcnt(2)
	v_pk_add_f32 v[14:15], v[4:5], 0 op_sel_hi:[1,0]
	v_pk_add_f32 v[16:17], v[2:3], 0 op_sel_hi:[1,0]
	ds_read_b128 v[2:5], v93 offset:16400
	s_waitcnt lgkmcnt(2)
	v_pk_add_f32 v[18:19], v[8:9], 0 op_sel_hi:[1,0]
	v_pk_add_f32 v[20:21], v[6:7], 0 op_sel_hi:[1,0]
	ds_read_b128 v[6:9], v93 offset:32768
	s_waitcnt lgkmcnt(2)
	v_pk_add_f32 v[14:15], v[14:15], v[12:13]
	v_pk_add_f32 v[16:17], v[16:17], v[10:11]
	s_waitcnt lgkmcnt(1)
	v_pk_add_f32 v[18:19], v[18:19], v[4:5]
	ds_read_b128 v[10:13], v93 offset:32784
	v_pk_add_f32 v[20:21], v[20:21], v[2:3]
	ds_read_b128 v[2:5], v93 offset:49152
	s_waitcnt lgkmcnt(2)
	v_pk_add_f32 v[14:15], v[14:15], v[8:9]
	v_pk_add_f32 v[16:17], v[16:17], v[6:7]
	ds_read_b128 v[6:9], v93 offset:49168
	s_waitcnt lgkmcnt(2)
	v_pk_add_f32 v[18:19], v[18:19], v[12:13]
	v_pk_add_f32 v[20:21], v[20:21], v[10:11]
	s_waitcnt lgkmcnt(1)
	v_pk_add_f32 v[14:15], v[14:15], v[4:5]
	ds_read_b128 v[10:13], v94
	v_pk_add_f32 v[16:17], v[16:17], v[2:3]
	ds_read_b128 v[2:5], v95
	s_waitcnt lgkmcnt(2)
	v_pk_add_f32 v[18:19], v[18:19], v[8:9]
	v_pk_add_f32 v[20:21], v[20:21], v[6:7]
	ds_read_b128 v[6:9], v96
	s_waitcnt lgkmcnt(2)
	v_pk_add_f32 v[14:15], v[14:15], v[12:13]
	v_pk_add_f32 v[16:17], v[16:17], v[10:11]
	s_waitcnt lgkmcnt(1)
	v_pk_add_f32 v[18:19], v[18:19], v[4:5]
	ds_read_b128 v[10:13], v97
	v_pk_add_f32 v[20:21], v[20:21], v[2:3]
	ds_read_b128 v[2:5], v98
	s_waitcnt lgkmcnt(2)
	v_pk_add_f32 v[14:15], v[14:15], v[8:9]
	v_pk_add_f32 v[16:17], v[16:17], v[6:7]
	ds_read_b128 v[6:9], v99
	s_waitcnt lgkmcnt(2)
	v_pk_add_f32 v[18:19], v[18:19], v[12:13]
	v_pk_add_f32 v[20:21], v[20:21], v[10:11]
	s_waitcnt lgkmcnt(1)
	v_pk_add_f32 v[14:15], v[14:15], v[4:5]
	ds_read_b128 v[10:13], v100
	v_pk_add_f32 v[16:17], v[16:17], v[2:3]
	ds_read_b128 v[2:5], v101
	s_waitcnt lgkmcnt(2)
	v_pk_add_f32 v[8:9], v[18:19], v[8:9]
	v_pk_add_f32 v[6:7], v[20:21], v[6:7]
	s_waitcnt lgkmcnt(1)
	v_pk_add_f32 v[12:13], v[14:15], v[12:13]
	v_pk_add_f32 v[10:11], v[16:17], v[10:11]
	s_waitcnt lgkmcnt(0)
	v_pk_add_f32 v[8:9], v[8:9], v[4:5]
	v_pk_add_f32 v[4:5], v[6:7], v[2:3]
	v_add_u32_e32 v7, s11, v91
	v_lshl_or_b32 v6, s16, 6, v92
	v_cvt_pk_bf16_f32 v4, v4, v5
	v_cvt_pk_bf16_f32 v5, v8, v9
	v_mov_b64_e32 v[8:9], s[4:5]
	v_mad_i64_i32 v[8:9], s[16:17], v7, s9, v[8:9]
	v_ashrrev_i32_e32 v7, 31, v6
	v_cvt_pk_bf16_f32 v2, v10, v11
	v_cvt_pk_bf16_f32 v3, v12, v13
	v_lshl_add_u64 v[6:7], v[6:7], 1, v[8:9]
	global_store_dwordx4 v[6:7], v[2:5], off
	s_cbranch_scc1 .LBB0_1535

.LBB0_1620:
	v_lshl_add_u64 v[100:101], v[82:83], 0, v[72:73]
	v_add_co_u32_e32 v156, vcc, s8, v100
	v_lshl_add_u64 v[152:153], v[82:83], 0, v[74:75]
	s_nop 0
	v_addc_co_u32_e32 v157, vcc, 0, v101, vcc
	v_add_co_u32_e32 v158, vcc, s9, v100
	v_lshl_add_u64 v[154:155], v[82:83], 0, v[76:77]
	s_nop 0
	v_addc_co_u32_e32 v159, vcc, 0, v101, vcc
	v_add_co_u32_e32 v160, vcc, s10, v100
	v_lshl_add_u64 v[164:165], v[82:83], 0, v[80:81]
	s_nop 0
	v_addc_co_u32_e32 v161, vcc, 0, v101, vcc
	v_add_co_u32_e32 v162, vcc, s11, v100
	v_lshl_add_u64 v[166:167], v[82:83], 0, v[78:79]
	s_nop 0
	v_addc_co_u32_e32 v163, vcc, 0, v101, vcc
	global_load_dwordx4 v[104:107], v[152:153], off offset:-128
	global_load_dwordx4 v[108:111], v[152:153], off offset:-64
	global_load_dwordx4 v[112:115], v[156:157], off
	global_load_dwordx4 v[116:119], v[156:157], off offset:64
	global_load_dwordx4 v[120:123], v[158:159], off offset:1024
	global_load_dwordx4 v[124:127], v[158:159], off offset:1088
	global_load_dwordx4 v[128:131], v[160:161], off
	global_load_dwordx4 v[132:135], v[160:161], off offset:64
	global_load_dwordx4 v[136:139], v[162:163], off offset:1024
	global_load_dwordx4 v[140:143], v[162:163], off offset:1088
	s_addk_i32 s19, 0x80
	s_cmpk_lt_u32 s19, 0xe0
	v_lshl_add_u64 v[82:83], v[82:83], 0, s[4:5]
	global_load_dwordx4 v[144:147], v[154:155], off offset:-128
	global_load_dwordx4 v[148:151], v[154:155], off offset:-64
	global_load_dwordx4 v[252:255], v[164:165], off offset:-128
	global_load_dwordx4 v[248:251], v[164:165], off offset:-64
	global_load_dwordx4 v[244:247], v[166:167], off offset:-128
	global_load_dwordx4 v[240:243], v[166:167], off offset:-64
	global_load_dwordx4 v[236:239], v[152:153], off
	global_load_dwordx4 v[232:235], v[152:153], off offset:64
	global_load_dwordx4 v[228:231], v[156:157], off offset:128
	global_load_dwordx4 v[224:227], v[156:157], off offset:192
	global_load_dwordx4 v[220:223], v[158:159], off offset:1152
	global_load_dwordx4 v[216:219], v[158:159], off offset:1216
	global_load_dwordx4 v[212:215], v[160:161], off offset:128
	global_load_dwordx4 v[208:211], v[160:161], off offset:192
	global_load_dwordx4 v[204:207], v[162:163], off offset:1152
	global_load_dwordx4 v[200:203], v[162:163], off offset:1216
	global_load_dwordx4 v[196:199], v[154:155], off
	global_load_dwordx4 v[192:195], v[154:155], off offset:64
	global_load_dwordx4 v[188:191], v[164:165], off
	global_load_dwordx4 v[184:187], v[164:165], off offset:64
	global_load_dwordx4 v[180:183], v[166:167], off
	global_load_dwordx4 v[176:179], v[166:167], off offset:64
	s_waitcnt vmcnt(29)
	v_mfma_f32_16x16x32_bf16 v[58:61], v[112:115], v[104:107], v[58:61]
	s_waitcnt vmcnt(27)
	v_mfma_f32_16x16x32_bf16 v[50:53], v[120:123], v[104:107], v[50:53]
	s_waitcnt vmcnt(25)
	v_mfma_f32_16x16x32_bf16 v[62:65], v[128:131], v[104:107], v[62:65]
	s_waitcnt vmcnt(23)
	v_mfma_f32_16x16x32_bf16 v[54:57], v[136:139], v[104:107], v[54:57]
	v_mfma_f32_16x16x32_bf16 v[58:61], v[116:119], v[108:111], v[58:61]
	v_mfma_f32_16x16x32_bf16 v[50:53], v[124:127], v[108:111], v[50:53]
	v_mfma_f32_16x16x32_bf16 v[62:65], v[132:135], v[108:111], v[62:65]
	s_waitcnt vmcnt(22)
	v_mfma_f32_16x16x32_bf16 v[54:57], v[140:143], v[108:111], v[54:57]
	s_waitcnt vmcnt(21)
	v_mfma_f32_16x16x32_bf16 v[46:49], v[112:115], v[144:147], v[46:49]
	v_mfma_f32_16x16x32_bf16 v[42:45], v[120:123], v[144:147], v[42:45]
	v_mfma_f32_16x16x32_bf16 v[38:41], v[128:131], v[144:147], v[38:41]
	v_mfma_f32_16x16x32_bf16 v[34:37], v[136:139], v[144:147], v[34:37]
	s_waitcnt vmcnt(20)
	v_mfma_f32_16x16x32_bf16 v[46:49], v[116:119], v[148:151], v[46:49]
	v_mfma_f32_16x16x32_bf16 v[42:45], v[124:127], v[148:151], v[42:45]
	v_mfma_f32_16x16x32_bf16 v[38:41], v[132:135], v[148:151], v[38:41]
	v_mfma_f32_16x16x32_bf16 v[34:37], v[140:143], v[148:151], v[34:37]
	s_waitcnt vmcnt(19)
	v_mfma_f32_16x16x32_bf16 v[30:33], v[112:115], v[252:255], v[30:33]
	v_mfma_f32_16x16x32_bf16 v[26:29], v[120:123], v[252:255], v[26:29]
	v_mfma_f32_16x16x32_bf16 v[22:25], v[128:131], v[252:255], v[22:25]
	v_mfma_f32_16x16x32_bf16 v[18:21], v[136:139], v[252:255], v[18:21]
	s_waitcnt vmcnt(17)
	v_mfma_f32_16x16x32_bf16 v[14:17], v[112:115], v[244:247], v[14:17]
	v_mfma_f32_16x16x32_bf16 v[10:13], v[120:123], v[244:247], v[10:13]
	v_mfma_f32_16x16x32_bf16 v[6:9], v[128:131], v[244:247], v[6:9]
	v_mfma_f32_16x16x32_bf16 v[2:5], v[136:139], v[244:247], v[2:5]
	v_mfma_f32_16x16x32_bf16 v[30:33], v[116:119], v[248:251], v[30:33]
	v_mfma_f32_16x16x32_bf16 v[26:29], v[124:127], v[248:251], v[26:29]
	v_mfma_f32_16x16x32_bf16 v[22:25], v[132:135], v[248:251], v[22:25]
	v_mfma_f32_16x16x32_bf16 v[18:21], v[140:143], v[248:251], v[18:21]
	s_waitcnt vmcnt(16)
	v_mfma_f32_16x16x32_bf16 v[14:17], v[116:119], v[240:243], v[14:17]
	v_mfma_f32_16x16x32_bf16 v[10:13], v[124:127], v[240:243], v[10:13]
	v_mfma_f32_16x16x32_bf16 v[6:9], v[132:135], v[240:243], v[6:9]
	v_mfma_f32_16x16x32_bf16 v[2:5], v[140:143], v[240:243], v[2:5]
	s_waitcnt vmcnt(13)
	v_mfma_f32_16x16x32_bf16 v[58:61], v[228:231], v[236:239], v[58:61]
	s_waitcnt vmcnt(11)
	v_mfma_f32_16x16x32_bf16 v[50:53], v[220:223], v[236:239], v[50:53]
	s_waitcnt vmcnt(9)
	v_mfma_f32_16x16x32_bf16 v[62:65], v[212:215], v[236:239], v[62:65]
	s_waitcnt vmcnt(7)
	v_mfma_f32_16x16x32_bf16 v[54:57], v[204:207], v[236:239], v[54:57]
	s_waitcnt vmcnt(5)
	v_mfma_f32_16x16x32_bf16 v[46:49], v[228:231], v[196:199], v[46:49]
	v_mfma_f32_16x16x32_bf16 v[42:45], v[220:223], v[196:199], v[42:45]
	v_mfma_f32_16x16x32_bf16 v[38:41], v[212:215], v[196:199], v[38:41]
	v_mfma_f32_16x16x32_bf16 v[34:37], v[204:207], v[196:199], v[34:37]
	s_waitcnt vmcnt(3)
	v_mfma_f32_16x16x32_bf16 v[30:33], v[228:231], v[188:191], v[30:33]
	v_mfma_f32_16x16x32_bf16 v[26:29], v[220:223], v[188:191], v[26:29]
	v_mfma_f32_16x16x32_bf16 v[22:25], v[212:215], v[188:191], v[22:25]
	v_mfma_f32_16x16x32_bf16 v[18:21], v[204:207], v[188:191], v[18:21]
	s_waitcnt vmcnt(1)
	v_mfma_f32_16x16x32_bf16 v[14:17], v[228:231], v[180:183], v[14:17]
	v_mfma_f32_16x16x32_bf16 v[10:13], v[220:223], v[180:183], v[10:13]
	v_mfma_f32_16x16x32_bf16 v[6:9], v[212:215], v[180:183], v[6:9]
	v_mfma_f32_16x16x32_bf16 v[2:5], v[204:207], v[180:183], v[2:5]
	v_mfma_f32_16x16x32_bf16 v[58:61], v[224:227], v[232:235], v[58:61]
	v_mfma_f32_16x16x32_bf16 v[50:53], v[216:219], v[232:235], v[50:53]
	v_mfma_f32_16x16x32_bf16 v[62:65], v[208:211], v[232:235], v[62:65]
	v_mfma_f32_16x16x32_bf16 v[54:57], v[200:203], v[232:235], v[54:57]
	v_mfma_f32_16x16x32_bf16 v[46:49], v[224:227], v[192:195], v[46:49]
	v_mfma_f32_16x16x32_bf16 v[42:45], v[216:219], v[192:195], v[42:45]
	v_mfma_f32_16x16x32_bf16 v[38:41], v[208:211], v[192:195], v[38:41]
	v_mfma_f32_16x16x32_bf16 v[34:37], v[200:203], v[192:195], v[34:37]
	v_mfma_f32_16x16x32_bf16 v[30:33], v[224:227], v[184:187], v[30:33]
	v_mfma_f32_16x16x32_bf16 v[26:29], v[216:219], v[184:187], v[26:29]
	v_mfma_f32_16x16x32_bf16 v[22:25], v[208:211], v[184:187], v[22:25]
	v_mfma_f32_16x16x32_bf16 v[18:21], v[200:203], v[184:187], v[18:21]
	s_waitcnt vmcnt(0)
	v_mfma_f32_16x16x32_bf16 v[14:17], v[224:227], v[176:179], v[14:17]
	v_mfma_f32_16x16x32_bf16 v[10:13], v[216:219], v[176:179], v[10:13]
	v_mfma_f32_16x16x32_bf16 v[6:9], v[208:211], v[176:179], v[6:9]
	v_mfma_f32_16x16x32_bf16 v[2:5], v[200:203], v[176:179], v[2:5]
	s_cbranch_scc1 .LBB0_1620
	s_barrier
	ds_write_b128 v98, v[58:61]
	ds_write_b128 v98, v[50:53] offset:16
	ds_write_b128 v98, v[62:65] offset:128
	ds_write_b128 v98, v[54:57] offset:144
	ds_write_b128 v98, v[46:49] offset:4096
	ds_write_b128 v98, v[42:45] offset:4112
	ds_write_b128 v98, v[38:41] offset:4224
	ds_write_b128 v98, v[34:37] offset:4240
	ds_write_b128 v98, v[30:33] offset:8192
	ds_write_b128 v98, v[26:29] offset:8208
	ds_write_b128 v98, v[22:25] offset:8320
	ds_write_b128 v98, v[18:21] offset:8336
	ds_write_b128 v98, v[14:17] offset:12288
	ds_write_b128 v98, v[10:13] offset:12304
	ds_write_b128 v98, v[6:9] offset:12416
	ds_write_b128 v98, v[2:5] offset:12432
	s_waitcnt lgkmcnt(0)
	s_barrier
	ds_read_b128 v[2:5], v85
	ds_read_b128 v[6:9], v85 offset:16
	ds_read_b128 v[10:13], v85 offset:16384
	s_addk_i32 s18, 0x4000
	s_lshl_b32 s17, s17, 5
	s_waitcnt lgkmcnt(2)
	v_pk_add_f32 v[14:15], v[4:5], 0 op_sel_hi:[1,0]
	v_pk_add_f32 v[16:17], v[2:3], 0 op_sel_hi:[1,0]
	ds_read_b128 v[2:5], v85 offset:16400
	s_waitcnt lgkmcnt(2)
	v_pk_add_f32 v[18:19], v[8:9], 0 op_sel_hi:[1,0]
	v_pk_add_f32 v[20:21], v[6:7], 0 op_sel_hi:[1,0]
	ds_read_b128 v[6:9], v85 offset:32768
	s_waitcnt lgkmcnt(2)
	v_pk_add_f32 v[14:15], v[14:15], v[12:13]
	v_pk_add_f32 v[16:17], v[16:17], v[10:11]
	s_waitcnt lgkmcnt(1)
	v_pk_add_f32 v[18:19], v[18:19], v[4:5]
	ds_read_b128 v[10:13], v85 offset:32784
	v_pk_add_f32 v[20:21], v[20:21], v[2:3]
	ds_read_b128 v[2:5], v85 offset:49152
	s_waitcnt lgkmcnt(2)
	v_pk_add_f32 v[14:15], v[14:15], v[8:9]
	v_pk_add_f32 v[16:17], v[16:17], v[6:7]
	ds_read_b128 v[6:9], v85 offset:49168
	s_waitcnt lgkmcnt(2)
	v_pk_add_f32 v[18:19], v[18:19], v[12:13]
	v_pk_add_f32 v[20:21], v[20:21], v[10:11]
	s_waitcnt lgkmcnt(1)
	v_pk_add_f32 v[14:15], v[14:15], v[4:5]
	ds_read_b128 v[10:13], v86
	v_pk_add_f32 v[16:17], v[16:17], v[2:3]
	ds_read_b128 v[2:5], v87
	s_waitcnt lgkmcnt(2)
	v_pk_add_f32 v[18:19], v[18:19], v[8:9]
	v_pk_add_f32 v[20:21], v[20:21], v[6:7]
	ds_read_b128 v[6:9], v88
	s_waitcnt lgkmcnt(2)
	v_pk_add_f32 v[14:15], v[14:15], v[12:13]
	v_pk_add_f32 v[16:17], v[16:17], v[10:11]
	s_waitcnt lgkmcnt(1)
	v_pk_add_f32 v[18:19], v[18:19], v[4:5]
	ds_read_b128 v[10:13], v89
	v_pk_add_f32 v[20:21], v[20:21], v[2:3]
	ds_read_b128 v[2:5], v90
	s_waitcnt lgkmcnt(2)
	v_pk_add_f32 v[14:15], v[14:15], v[8:9]
	v_pk_add_f32 v[16:17], v[16:17], v[6:7]
	ds_read_b128 v[6:9], v91
	s_waitcnt lgkmcnt(2)
	v_pk_add_f32 v[18:19], v[18:19], v[12:13]
	v_pk_add_f32 v[20:21], v[20:21], v[10:11]
	s_waitcnt lgkmcnt(1)
	v_pk_add_f32 v[14:15], v[14:15], v[4:5]
	ds_read_b128 v[10:13], v92
	v_pk_add_f32 v[16:17], v[16:17], v[2:3]
	ds_read_b128 v[2:5], v93
	s_waitcnt lgkmcnt(2)
	v_pk_add_f32 v[8:9], v[18:19], v[8:9]
	v_pk_add_f32 v[6:7], v[20:21], v[6:7]
	s_sub_i32 s17, s16, s17
	s_waitcnt lgkmcnt(1)
	v_pk_add_f32 v[12:13], v[14:15], v[12:13]
	s_waitcnt lgkmcnt(0)
	v_pk_add_f32 v[8:9], v[8:9], v[4:5]
	v_pk_add_f32 v[4:5], v[6:7], v[2:3]
	v_add_u32_e32 v6, s18, v1
	v_ashrrev_i32_e32 v7, 31, v6
	v_lshl_or_b32 v14, s17, 6, v84
	v_lshlrev_b64 v[6:7], 12, v[6:7]
	v_pk_add_f32 v[10:11], v[16:17], v[10:11]
	v_lshl_add_u64 v[6:7], s[14:15], 0, v[6:7]
	v_ashrrev_i32_e32 v15, 31, v14
	s_add_i32 s16, s16, s26
	v_cvt_pk_bf16_f32 v2, v10, v11
	v_cvt_pk_bf16_f32 v3, v12, v13
	v_cvt_pk_bf16_f32 v4, v4, v5
	v_cvt_pk_bf16_f32 v5, v8, v9
	v_lshl_add_u64 v[6:7], v[14:15], 1, v[6:7]
	s_cmpk_lt_i32 s16, 0x100
	global_store_dwordx4 v[6:7], v[2:5], off
	s_cbranch_scc1 .LBB0_1619
